# speedup vs baseline: 1.0050x; 1.0027x over previous
.LBB3_19:
	v_lshrrev_b32_e32 v1, 6, v0
	v_bfe_u32 v36, v0, 2, 4
	v_lshlrev_b32_e32 v37, 4, v0
	v_and_b32_e32 v37, 48, v37
	v_lshl_add_u32 v10, v1, 7, v36
	v_lshl_add_u32 v10, v10, 9, v37
	v_mul_u32_u24_e32 v1, 0x410, v1
	v_lshl_add_u32 v36, v36, 6, v37
	v_add_u32_e32 v11, v1, v36
	s_waitcnt lgkmcnt(0)
	s_barrier
	ds_read_b128 v[2:5], v11
	ds_read_b128 v[6:9], v11 offset:4160
	ds_read_b128 v[12:15], v11 offset:8320
	ds_read_b128 v[16:19], v11 offset:12480
	ds_read_b128 v[20:23], v11 offset:16640
	ds_read_b128 v[24:27], v11 offset:20800
	ds_read_b128 v[28:31], v11 offset:24960
	ds_read_b128 v[32:35], v11 offset:29120
	s_lshl_b32 s0, s20, 2
	s_add_u32 s0, s14, s0
	s_addc_u32 s1, s15, 0
	s_lshl_b32 s2, s18, 7
	s_add_i32 s2, s2, s19
	s_lshl_b32 s2, s2, 9
	s_add_u32 s24, s0, s2
	s_addc_u32 s25, s1, 0
	s_add_u32 s26, s24, 0x40000
	s_addc_u32 s27, s25, 0
	s_add_u32 s28, s26, 0x40000
	s_addc_u32 s29, s27, 0
	s_add_u32 s30, s28, 0x40000
	s_addc_u32 s31, s29, 0
	s_add_u32 s32, s30, 0x40000
	s_addc_u32 s33, s31, 0
	s_add_u32 s34, s32, 0x40000
	s_addc_u32 s35, s33, 0
	s_add_u32 s36, s34, 0x40000
	s_addc_u32 s37, s35, 0
	s_add_u32 s38, s36, 0x40000
	s_addc_u32 s39, s37, 0
	s_waitcnt lgkmcnt(7)
	global_store_dwordx4 v10, v[2:5], s[24:25] nt
	s_waitcnt lgkmcnt(6)
	global_store_dwordx4 v10, v[6:9], s[26:27] nt
	s_waitcnt lgkmcnt(5)
	global_store_dwordx4 v10, v[12:15], s[28:29] nt
	s_waitcnt lgkmcnt(4)
	global_store_dwordx4 v10, v[16:19], s[30:31] nt
	s_waitcnt lgkmcnt(3)
	global_store_dwordx4 v10, v[20:23], s[32:33] nt
	s_waitcnt lgkmcnt(2)
	global_store_dwordx4 v10, v[24:27], s[34:35] nt
	s_waitcnt lgkmcnt(1)
	global_store_dwordx4 v10, v[28:31], s[36:37] nt
	s_waitcnt lgkmcnt(0)
	global_store_dwordx4 v10, v[32:35], s[38:39] nt
